# hybrid K1 (15 private chunks + atomic chunk queues) + final_kernel loads hoisted before BN-stats barrier + agg2 kernarg hoist
# speedup vs baseline: 1.0381x; 1.0074x over previous
amdhsa.kernels:
  - .agpr_count:     0
    .args:
      - .actual_access:  read_only
        .address_space:  global
        .offset:         0
        .size:           8
        .value_kind:     global_buffer
      - .actual_access:  read_only
        .address_space:  global
        .offset:         8
        .size:           8
        .value_kind:     global_buffer
      - .actual_access:  read_only
        .address_space:  global
        .offset:         16
        .size:           8
        .value_kind:     global_buffer
      - .actual_access:  write_only
        .address_space:  global
        .offset:         24
        .size:           8
        .value_kind:     global_buffer
      - .address_space:  global
        .offset:         32
        .size:           8
        .value_kind:     global_buffer
      - .address_space:  global
        .offset:         40
        .size:           8
        .value_kind:     global_buffer
      - .actual_access:  write_only
        .address_space:  global
        .offset:         48
        .size:           8
        .value_kind:     global_buffer
      - .actual_access:  write_only
        .address_space:  global
        .offset:         56
        .size:           8
        .value_kind:     global_buffer
    .group_segment_fixed_size: 37392
    .kernarg_segment_align: 8
    .kernarg_segment_size: 64
    .language:       OpenCL C
    .language_version:
      - 2
      - 0
    .max_flat_workgroup_size: 256
    .name:           _Z9k1_kernelPKfS0_S0_PDF16_PiPfP15HIP_vector_typeIiLj2EES6_
    .private_segment_fixed_size: 0
    .sgpr_count:     32
    .sgpr_spill_count: 0
    .symbol:         _Z9k1_kernelPKfS0_S0_PDF16_PiPfP15HIP_vector_typeIiLj2EES6_.kd
    .uniform_work_group_size: 1
    .uses_dynamic_stack: false
    .vgpr_count:     140
    .vgpr_spill_count: 0
    .wavefront_size: 64
  - .agpr_count:     0
    .args:
      - .actual_access:  read_only
        .address_space:  global
        .offset:         0
        .size:           8
        .value_kind:     global_buffer
      - .actual_access:  read_only
        .address_space:  global
        .offset:         8
        .size:           8
        .value_kind:     global_buffer
      - .actual_access:  read_only
        .address_space:  global
        .offset:         16
        .size:           8
        .value_kind:     global_buffer
      - .actual_access:  read_only
        .address_space:  global
        .offset:         24
        .size:           8
        .value_kind:     global_buffer
      - .actual_access:  read_only
        .address_space:  global
        .offset:         32
        .size:           8
        .value_kind:     global_buffer
      - .actual_access:  read_only
        .address_space:  global
        .offset:         40
        .size:           8
        .value_kind:     global_buffer
      - .actual_access:  read_only
        .address_space:  global
        .offset:         48
        .size:           8
        .value_kind:     global_buffer
      - .actual_access:  read_only
        .address_space:  global
        .offset:         56
        .size:           8
        .value_kind:     global_buffer
      - .actual_access:  read_only
        .address_space:  global
        .offset:         64
        .size:           8
        .value_kind:     global_buffer
      - .actual_access:  write_only
        .address_space:  global
        .offset:         72
        .size:           8
        .value_kind:     global_buffer
      - .address_space:  global
        .offset:         80
        .size:           8
        .value_kind:     global_buffer
    .group_segment_fixed_size: 44224
    .kernarg_segment_align: 8
    .kernarg_segment_size: 88
    .language:       OpenCL C
    .language_version:
      - 2
      - 0
    .max_flat_workgroup_size: 512
    .name:           _Z11agg2_kernelPKiPKfPK15HIP_vector_typeIiLj2EEPKDF16_S2_S2_S2_S2_S2_PfS9_
    .private_segment_fixed_size: 0
    .sgpr_count:     41
    .sgpr_spill_count: 0
    .symbol:         _Z11agg2_kernelPKiPKfPK15HIP_vector_typeIiLj2EEPKDF16_S2_S2_S2_S2_S2_PfS9_.kd
    .uniform_work_group_size: 1
    .uses_dynamic_stack: false
    .vgpr_count:     80
    .vgpr_spill_count: 0
    .wavefront_size: 64
  - .agpr_count:     0
    .args:
      - .actual_access:  read_only
        .address_space:  global
        .offset:         0
        .size:           8
        .value_kind:     global_buffer
      - .actual_access:  read_only
        .address_space:  global
        .offset:         8
        .size:           8
        .value_kind:     global_buffer
      - .actual_access:  read_only
        .address_space:  global
        .offset:         16
        .size:           8
        .value_kind:     global_buffer
      - .actual_access:  read_only
        .address_space:  global
        .offset:         24
        .size:           8
        .value_kind:     global_buffer
      - .actual_access:  write_only
        .address_space:  global
        .offset:         32
        .size:           8
        .value_kind:     global_buffer
      - .offset:         40
        .size:           4
        .value_kind:     hidden_block_count_x
      - .offset:         44
        .size:           4
        .value_kind:     hidden_block_count_y
      - .offset:         48
        .size:           4
        .value_kind:     hidden_block_count_z
      - .offset:         52
        .size:           2
        .value_kind:     hidden_group_size_x
      - .offset:         54
        .size:           2
        .value_kind:     hidden_group_size_y
      - .offset:         56
        .size:           2
        .value_kind:     hidden_group_size_z
      - .offset:         58
        .size:           2
        .value_kind:     hidden_remainder_x
      - .offset:         60
        .size:           2
        .value_kind:     hidden_remainder_y
      - .offset:         62
        .size:           2
        .value_kind:     hidden_remainder_z
      - .offset:         80
        .size:           8
        .value_kind:     hidden_global_offset_x
      - .offset:         88
        .size:           8
        .value_kind:     hidden_global_offset_y
      - .offset:         96
        .size:           8
        .value_kind:     hidden_global_offset_z
      - .offset:         104
        .size:           2
        .value_kind:     hidden_grid_dims
    .group_segment_fixed_size: 512
    .kernarg_segment_align: 8
    .kernarg_segment_size: 296
    .language:       OpenCL C
    .language_version:
      - 2
      - 0
    .max_flat_workgroup_size: 256
    .name:           _Z12final_kernelPKfS0_S0_S0_Pf
    .private_segment_fixed_size: 0
    .sgpr_count:     22
    .sgpr_spill_count: 0
    .symbol:         _Z12final_kernelPKfS0_S0_S0_Pf.kd
    .uniform_work_group_size: 1
    .uses_dynamic_stack: false
    .vgpr_count:     49
    .vgpr_spill_count: 0
    .wavefront_size: 64
  - .agpr_count:     0
    .args:
      - .actual_access:  read_only
        .address_space:  global
        .offset:         0
        .size:           8
        .value_kind:     global_buffer
      - .actual_access:  read_only
        .address_space:  global
        .offset:         8
        .size:           8
        .value_kind:     global_buffer
      - .address_space:  global
        .offset:         16
        .size:           8
        .value_kind:     global_buffer
      - .address_space:  global
        .offset:         24
        .size:           8
        .value_kind:     global_buffer
      - .actual_access:  read_only
        .address_space:  global
        .offset:         32
        .size:           8
        .value_kind:     global_buffer
      - .actual_access:  read_only
        .address_space:  global
        .offset:         40
        .size:           8
        .value_kind:     global_buffer
      - .actual_access:  write_only
        .address_space:  global
        .offset:         48
        .size:           8
        .value_kind:     global_buffer
      - .address_space:  global
        .offset:         56
        .size:           8
        .value_kind:     global_buffer
    .group_segment_fixed_size: 8192
    .kernarg_segment_align: 8
    .kernarg_segment_size: 64
    .language:       OpenCL C
    .language_version:
      - 2
      - 0
    .max_flat_workgroup_size: 512
    .name:           _Z10agg_kernelILi128ELb1EEvPKiPKfP15HIP_vector_typeIiLj2EES6_PKDF16_S3_PDF16_Pf
    .private_segment_fixed_size: 0
    .sgpr_count:     42
    .sgpr_spill_count: 0
    .symbol:         _Z10agg_kernelILi128ELb1EEvPKiPKfP15HIP_vector_typeIiLj2EES6_PKDF16_S3_PDF16_Pf.kd
    .uniform_work_group_size: 1
    .uses_dynamic_stack: false
    .vgpr_count:     80
    .vgpr_spill_count: 0
    .wavefront_size: 64
